# LSTM layer-1 main loop rewritten by hand: tile-0 x-part hoisted before the barrier, B fragments prefetched one segment ahead, in-place cell update
# speedup vs baseline: 1.0494x; 1.0494x over previous
	.section	.text._Z5k_gcnILi1EEvPKvPK15HIP_vector_typeIiLj2EEPfPKiS8_PKfPKDF16_SA_SA_SA_SA_S6_PDF16_S6_SD_SC_SA_,"axG",@progbits,_Z5k_gcnILi1EEvPKvPK15HIP_vector_typeIiLj2EEPfPKiS8_PKfPKDF16_SA_SA_SA_SA_S6_PDF16_S6_SD_SC_SA_,comdat
	.p2alignl 8, 3212836864

	.section	.text._Z5k_gcnILi2EEvPKvPK15HIP_vector_typeIiLj2EEPfPKiS8_PKfPKDF16_SA_SA_SA_SA_S6_PDF16_S6_SD_SC_SA_,"axG",@progbits,_Z5k_gcnILi2EEvPKvPK15HIP_vector_typeIiLj2EEPfPKiS8_PKfPKDF16_SA_SA_SA_SA_S6_PDF16_S6_SD_SC_SA_,comdat
	.p2alignl 8, 3212836864

_Z6k_lstmILi256ELi10ELb1ELb0EEvPKDF16_S1_S1_PKfPDF16_S1_S1_S1_S3_S3_S3_PfS5_:
	v_lshrrev_b32_e32 v195, 6, v0
	v_and_b32_e32 v205, 15, v0
	v_bfe_u32 v196, v0, 4, 2
	s_cmpk_lt_u32 s2, 0xd1
	s_mov_b64 s[4:5], -1
	s_cbranch_scc0 .LBB6_33
	s_load_dwordx4 s[4:7], s[0:1], 0x10
	s_load_dwordx2 s[8:9], s[0:1], 0x0
	s_load_dwordx2 s[10:11], s[0:1], 0x20
	v_and_b32_e32 v1, 63, v0
	v_lshrrev_b32_e32 v253, 6, v0
	v_mul_u32_u24_e32 v254, 0xc000, v253
	v_lshl_add_u32 v254, v1, 4, v254
	v_lshlrev_b32_e32 v255, 13, v253
	v_lshl_add_u32 v255, v1, 4, v255
	s_waitcnt lgkmcnt(0)
	v_add_u32_e32 v1, 0x0, v254
	global_load_dwordx4 v[2:5], v1, s[4:5] offset:0
	global_load_dwordx4 v[6:9], v1, s[4:5] offset:1024
	global_load_dwordx4 v[10:13], v1, s[4:5] offset:2048
	global_load_dwordx4 v[14:17], v1, s[4:5] offset:3072
	v_add_u32_e32 v1, 0x1000, v254
	global_load_dwordx4 v[18:21], v1, s[4:5] offset:0
	global_load_dwordx4 v[22:25], v1, s[4:5] offset:1024
	global_load_dwordx4 v[26:29], v1, s[4:5] offset:2048
	global_load_dwordx4 v[30:33], v1, s[4:5] offset:3072
	v_add_u32_e32 v1, 0x2000, v254
	global_load_dwordx4 v[34:37], v1, s[4:5] offset:0
	global_load_dwordx4 v[38:41], v1, s[4:5] offset:1024
	global_load_dwordx4 v[42:45], v1, s[4:5] offset:2048
	global_load_dwordx4 v[46:49], v1, s[4:5] offset:3072
	v_add_u32_e32 v1, 0x3000, v254
	global_load_dwordx4 v[50:53], v1, s[4:5] offset:0
	global_load_dwordx4 v[54:57], v1, s[4:5] offset:1024
	global_load_dwordx4 v[58:61], v1, s[4:5] offset:2048
	global_load_dwordx4 v[62:65], v1, s[4:5] offset:3072
	v_add_u32_e32 v1, 0x4000, v254
	global_load_dwordx4 v[66:69], v1, s[4:5] offset:0
	global_load_dwordx4 v[70:73], v1, s[4:5] offset:1024
	global_load_dwordx4 v[74:77], v1, s[4:5] offset:2048
	global_load_dwordx4 v[78:81], v1, s[4:5] offset:3072
	v_add_u32_e32 v1, 0x5000, v254
	global_load_dwordx4 v[82:85], v1, s[4:5] offset:0
	global_load_dwordx4 v[86:89], v1, s[4:5] offset:1024
	global_load_dwordx4 v[90:93], v1, s[4:5] offset:2048
	global_load_dwordx4 v[94:97], v1, s[4:5] offset:3072
	v_add_u32_e32 v1, 0x8000, v254
	global_load_dwordx4 v[98:101], v1, s[4:5] offset:0
	global_load_dwordx4 v[102:105], v1, s[4:5] offset:1024
	global_load_dwordx4 v[106:109], v1, s[4:5] offset:2048
	global_load_dwordx4 v[110:113], v1, s[4:5] offset:3072
	v_add_u32_e32 v1, 0x9000, v254
	global_load_dwordx4 v[114:117], v1, s[4:5] offset:0
	global_load_dwordx4 v[118:121], v1, s[4:5] offset:1024
	global_load_dwordx4 v[122:125], v1, s[4:5] offset:2048
	global_load_dwordx4 v[126:129], v1, s[4:5] offset:3072
	v_add_u32_e32 v1, 0xa000, v254
	global_load_dwordx4 v[130:133], v1, s[4:5] offset:0
	global_load_dwordx4 v[134:137], v1, s[4:5] offset:1024
	global_load_dwordx4 v[138:141], v1, s[4:5] offset:2048
	global_load_dwordx4 v[142:145], v1, s[4:5] offset:3072
	v_add_u32_e32 v1, 0xb000, v254
	global_load_dwordx4 v[146:149], v1, s[4:5] offset:0
	global_load_dwordx4 v[150:153], v1, s[4:5] offset:1024
	global_load_dwordx4 v[154:157], v1, s[4:5] offset:2048
	global_load_dwordx4 v[158:161], v1, s[4:5] offset:3072
	v_add_u32_e32 v1, 0x6000, v254
	global_load_dwordx4 v[174:177], v1, s[4:5] offset:0
	global_load_dwordx4 v[178:181], v1, s[4:5] offset:1024
	global_load_dwordx4 v[182:185], v1, s[4:5] offset:2048
	global_load_dwordx4 v[186:189], v1, s[4:5] offset:3072
	v_add_u32_e32 v1, 0x7000, v254
	global_load_dwordx4 v[190:193], v1, s[4:5] offset:0
	global_load_dwordx4 v[194:197], v1, s[4:5] offset:1024
	global_load_dwordx4 v[198:201], v1, s[4:5] offset:2048
	global_load_dwordx4 v[202:205], v1, s[4:5] offset:3072
	v_lshlrev_b32_e32 v1, 2, v0
	global_load_dword v206, v1, s[6:7]
	v_add_u32_e32 v245, 0x22c00, v1
	s_mul_i32 s22, s2, 48
	v_lshrrev_b32_e32 v1, 5, v0
	v_and_b32_e32 v253, 15, v0
	v_lshlrev_b32_e32 v253, 4, v253
	v_and_b32_e32 v254, 16, v0
	v_mul_u32_u24_e32 v254, 0x271000, v254
	v_add_u32_e32 v253, v253, v254
	v_add_u32_e32 v254, s22, v1
	v_min_u32_e32 v246, 0x270f, v254
	v_lshl_add_u32 v246, v246, 8, v253
	v_add_u32_e32 v254, 16, v254
	v_min_u32_e32 v247, 0x270f, v254
	v_lshl_add_u32 v247, v247, 8, v253
	v_add_u32_e32 v254, 16, v254
	v_min_u32_e32 v248, 0x270f, v254
	v_lshl_add_u32 v248, v248, 8, v253
	v_and_b32_e32 v253, 31, v0
	v_mul_u32_u24_e32 v249, 0x210, v1
	v_lshl_add_u32 v249, v253, 4, v249
	v_add_u32_e32 v249, 0x10000, v249
	s_add_u32 s12, s8, 0x271000
	s_addc_u32 s13, s9, 0
	global_load_dwordx4 v[230:233], v246, s[8:9]
	global_load_dwordx4 v[234:237], v247, s[8:9]
	global_load_dwordx4 v[238:241], v248, s[8:9]
	global_load_dwordx4 v[210:213], v246, s[12:13]
	s_add_u32 s8, s8, 0x271000
	s_addc_u32 s9, s9, 0
	s_add_u32 s12, s12, 0x271000
	s_addc_u32 s13, s13, 0
	v_lshrrev_b32_e32 v1, 4, v0
	v_and_b32_e32 v253, 15, v0
	v_mul_u32_u24_e32 v250, 0x110, v1
	v_lshl_add_u32 v250, v253, 4, v250
	v_add_u32_e32 v250, 0x1c600, v250
	v_add_u32_e32 v254, s22, v1
	v_lshlrev_b32_e32 v251, 8, v254
	v_lshl_add_u32 v251, v253, 4, v251
	s_movk_i32 s23, 0x2710
	v_cmp_gt_u32_e64 s[18:19], s23, v254
	v_add_u32_e32 v254, 32, v254
	v_cmp_gt_u32_e64 s[20:21], s23, v254
	s_movk_i32 s23, 0x100
	v_cmp_gt_u32_e64 s[22:23], s23, v0
	s_nop 3
	s_and_b64 s[20:21], s[20:21], s[22:23]
	s_add_u32 s14, s10, 0x2000
	s_addc_u32 s15, s11, 0
	v_and_b32_e32 v1, 15, v0
	v_bfe_u32 v253, v0, 4, 2
	v_lshrrev_b32_e32 v254, 6, v0
	v_mul_u32_u24_e32 v242, 0x210, v1
	v_lshl_add_u32 v242, v253, 4, v242
	v_add_u32_e32 v242, 0x10000, v242
	v_mul_u32_u24_e32 v243, 0x110, v1
	v_add_u32_e32 v243, 0x1c600, v243
	v_lshl_add_u32 v244, v253, 3, v243
	v_lshl_add_u32 v244, v254, 5, v244
	v_lshl_add_u32 v243, v253, 4, v243
	v_mov_b32_e32 v214, 0
	v_mov_b32_e32 v215, 0
	v_mov_b32_e32 v216, 0
	v_mov_b32_e32 v217, 0
	v_mov_b32_e32 v162, 0
	v_mov_b32_e32 v163, 0
	v_mov_b32_e32 v164, 0
	v_mov_b32_e32 v165, 0
	v_mov_b32_e32 v166, 0
	v_mov_b32_e32 v167, 0
	v_mov_b32_e32 v168, 0
	v_mov_b32_e32 v169, 0
	v_mov_b32_e32 v170, 0
	v_mov_b32_e32 v171, 0
	v_mov_b32_e32 v172, 0
	v_mov_b32_e32 v173, 0
	v_mov_b32_e32 v252, 0x4038aa3b
	s_mov_b32 s16, 0xc0b8aa3b
	v_lshlrev_b32_e32 v1, 4, v0
	v_add_u32_e32 v1, 0x1c600, v1
	ds_write_b128 v1, v[214:217]
	ds_write_b128 v1, v[214:217] offset:8192
	s_waitcnt vmcnt(0)
	ds_write_b128 v255, v[174:177] offset:0
	ds_write_b128 v255, v[178:181] offset:1024
	ds_write_b128 v255, v[182:185] offset:2048
	ds_write_b128 v255, v[186:189] offset:3072
	ds_write_b128 v255, v[190:193] offset:4096
	ds_write_b128 v255, v[194:197] offset:5120
	ds_write_b128 v255, v[198:201] offset:6144
	ds_write_b128 v255, v[202:205] offset:7168
	ds_write_b32 v245, v206
	ds_write_b128 v249, v[230:233]
	ds_write_b128 v249, v[234:237] offset:8448
	ds_write_b128 v249, v[238:241] offset:16896
	ds_write_b128 v249, v[210:213] offset:25344
	v_lshlrev_b32_e32 v245, 6, v254
	v_lshl_add_u32 v245, v253, 4, v245
	v_add_u32_e32 v245, 0x22c00, v245
	s_waitcnt lgkmcnt(0)
	s_barrier
	ds_read_b128 v[214:217], v255 offset:0
	ds_read_b128 v[218:221], v255 offset:1024
	ds_read_b128 v[222:225], v255 offset:2048
	ds_read_b128 v[226:229], v255 offset:3072
	ds_read_b128 v[174:177], v245 offset:0
	ds_read_b128 v[178:181], v245 offset:512
	ds_read_b128 v[182:185], v245 offset:1024
	ds_read_b128 v[186:189], v245 offset:1536
	ds_read_b128 v[206:209], v242 offset:0
	s_waitcnt lgkmcnt(0)
	ds_read_b128 v[210:213], v242 offset:64
	v_mfma_f32_16x16x32_f16 v[174:177], v[2:5], v[206:209], v[174:177]
	v_mfma_f32_16x16x32_f16 v[178:181], v[6:9], v[206:209], v[178:181]
	v_mfma_f32_16x16x32_f16 v[182:185], v[10:13], v[206:209], v[182:185]
	v_mfma_f32_16x16x32_f16 v[186:189], v[14:17], v[206:209], v[186:189]
	s_waitcnt lgkmcnt(0)
	ds_read_b128 v[206:209], v242 offset:384
	v_mfma_f32_16x16x32_f16 v[174:177], v[18:21], v[210:213], v[174:177]
	v_mfma_f32_16x16x32_f16 v[178:181], v[22:25], v[210:213], v[178:181]
	v_mfma_f32_16x16x32_f16 v[182:185], v[26:29], v[210:213], v[182:185]
	v_mfma_f32_16x16x32_f16 v[186:189], v[30:33], v[210:213], v[186:189]
	s_waitcnt lgkmcnt(0)
	ds_read_b128 v[210:213], v242 offset:128
	v_mfma_f32_16x16x32_f16 v[174:177], v[214:217], v[206:209], v[174:177]
	ds_read_b128 v[214:217], v255 offset:4096
	v_mfma_f32_16x16x32_f16 v[178:181], v[218:221], v[206:209], v[178:181]
	ds_read_b128 v[218:221], v255 offset:5120
	v_mfma_f32_16x16x32_f16 v[182:185], v[222:225], v[206:209], v[182:185]
	ds_read_b128 v[222:225], v255 offset:6144
	v_mfma_f32_16x16x32_f16 v[186:189], v[226:229], v[206:209], v[186:189]
	ds_read_b128 v[226:229], v255 offset:7168
	ds_read_b128 v[190:193], v245 offset:0
	s_waitcnt lgkmcnt(5)
	ds_read_b128 v[206:209], v242 offset:192
	v_mfma_f32_16x16x32_f16 v[174:177], v[34:37], v[210:213], v[174:177]
	v_mfma_f32_16x16x32_f16 v[178:181], v[38:41], v[210:213], v[178:181]
	v_mfma_f32_16x16x32_f16 v[182:185], v[42:45], v[210:213], v[182:185]
	v_mfma_f32_16x16x32_f16 v[186:189], v[46:49], v[210:213], v[186:189]
	s_waitcnt lgkmcnt(0)
	ds_read_b128 v[210:213], v242 offset:256
	v_mfma_f32_16x16x32_f16 v[174:177], v[50:53], v[206:209], v[174:177]
	ds_read_b128 v[194:197], v245 offset:512
	v_mfma_f32_16x16x32_f16 v[178:181], v[54:57], v[206:209], v[178:181]
	v_mfma_f32_16x16x32_f16 v[182:185], v[58:61], v[206:209], v[182:185]
	v_mfma_f32_16x16x32_f16 v[186:189], v[62:65], v[206:209], v[186:189]
	s_waitcnt lgkmcnt(1)
	ds_read_b128 v[206:209], v242 offset:448
	v_mfma_f32_16x16x32_f16 v[174:177], v[66:69], v[210:213], v[174:177]
	v_mfma_f32_16x16x32_f16 v[178:181], v[70:73], v[210:213], v[178:181]
	v_mfma_f32_16x16x32_f16 v[182:185], v[74:77], v[210:213], v[182:185]
	ds_read_b128 v[198:201], v245 offset:1024
	v_mfma_f32_16x16x32_f16 v[186:189], v[78:81], v[210:213], v[186:189]
	s_waitcnt lgkmcnt(1)
	ds_read_b128 v[210:213], v242 offset:320
	v_mfma_f32_16x16x32_f16 v[174:177], v[214:217], v[206:209], v[174:177]
	ds_read_b128 v[214:217], v255 offset:0
	v_mfma_f32_16x16x32_f16 v[178:181], v[218:221], v[206:209], v[178:181]
	ds_read_b128 v[218:221], v255 offset:1024
	v_mfma_f32_16x16x32_f16 v[182:185], v[222:225], v[206:209], v[182:185]
	ds_read_b128 v[222:225], v255 offset:2048
	v_mfma_f32_16x16x32_f16 v[186:189], v[226:229], v[206:209], v[186:189]
	ds_read_b128 v[226:229], v255 offset:3072
	ds_read_b128 v[202:205], v245 offset:1536
	s_waitcnt lgkmcnt(5)
	v_mfma_f32_16x16x32_f16 v[174:177], v[82:85], v[210:213], v[174:177]
	v_mfma_f32_16x16x32_f16 v[178:181], v[86:89], v[210:213], v[178:181]
	v_mfma_f32_16x16x32_f16 v[182:185], v[90:93], v[210:213], v[182:185]
	v_mfma_f32_16x16x32_f16 v[186:189], v[94:97], v[210:213], v[186:189]
	s_waitcnt lgkmcnt(0)
	s_mov_b32 s17, 0
	s_barrier
.Llstm1_loop:
	ds_read_b128 v[206:209], v243 offset:0
	ds_read_b128 v[230:233], v250 offset:0
	s_mov_b64 exec, s[20:21]
	ds_read_b128 v[234:237], v250 offset:8704
	s_mov_b64 exec, -1
	s_waitcnt lgkmcnt(2)
	ds_read_b128 v[210:213], v243 offset:64
	v_mfma_f32_16x16x32_f16 v[174:177], v[98:101], v[206:209], v[174:177]
	v_mfma_f32_16x16x32_f16 v[178:181], v[102:105], v[206:209], v[178:181]
	v_mfma_f32_16x16x32_f16 v[182:185], v[106:109], v[206:209], v[182:185]
	v_mfma_f32_16x16x32_f16 v[186:189], v[110:113], v[206:209], v[186:189]
	s_waitcnt lgkmcnt(1)
	s_cmp_eq_u32 s17, 0
	s_cbranch_scc1 .Lskipy78
	s_mov_b64 exec, s[18:19]
	global_store_dwordx4 v251, v[230:233], s[10:11]
	s_mov_b64 exec, s[20:21]
	global_store_dwordx4 v251, v[234:237], s[14:15]
	s_mov_b64 exec, -1
	s_add_u32 s10, s10, 0x271000
	s_addc_u32 s11, s11, 0
	s_add_u32 s14, s14, 0x271000
	s_addc_u32 s15, s15, 0
.Lskipy78:
	s_waitcnt lgkmcnt(0)
	ds_read_b128 v[206:209], v243 offset:128
	v_mfma_f32_16x16x32_f16 v[174:177], v[114:117], v[210:213], v[174:177]
	v_mfma_f32_16x16x32_f16 v[178:181], v[118:121], v[210:213], v[178:181]
	global_load_dwordx4 v[230:233], v246, s[12:13]
	v_mfma_f32_16x16x32_f16 v[182:185], v[122:125], v[210:213], v[182:185]
	v_mfma_f32_16x16x32_f16 v[186:189], v[126:129], v[210:213], v[186:189]
	global_load_dwordx4 v[234:237], v247, s[8:9]
	s_waitcnt lgkmcnt(0)
	ds_read_b128 v[210:213], v243 offset:192
	v_mfma_f32_16x16x32_f16 v[174:177], v[130:133], v[206:209], v[174:177]
	global_load_dwordx4 v[238:241], v248, s[8:9]
	v_mfma_f32_16x16x32_f16 v[178:181], v[134:137], v[206:209], v[178:181]
	v_mfma_f32_16x16x32_f16 v[182:185], v[138:141], v[206:209], v[182:185]
	s_add_u32 s8, s8, 0x271000
	v_mfma_f32_16x16x32_f16 v[186:189], v[142:145], v[206:209], v[186:189]
	s_waitcnt lgkmcnt(0)
	ds_read_b128 v[206:209], v242 offset:8448
	v_mfma_f32_16x16x32_f16 v[174:177], v[146:149], v[210:213], v[174:177]
	s_addc_u32 s9, s9, 0
	v_mfma_f32_16x16x32_f16 v[178:181], v[150:153], v[210:213], v[178:181]
	v_mfma_f32_16x16x32_f16 v[182:185], v[154:157], v[210:213], v[182:185]
	s_add_u32 s12, s12, 0x271000
	v_mfma_f32_16x16x32_f16 v[186:189], v[158:161], v[210:213], v[186:189]
	s_addc_u32 s13, s13, 0
	s_waitcnt lgkmcnt(0)
	ds_read_b128 v[210:213], v242 offset:8512
	v_mfma_f32_16x16x32_f16 v[190:193], v[2:5], v[206:209], v[190:193]
	v_mfma_f32_16x16x32_f16 v[194:197], v[6:9], v[206:209], v[194:197]
	v_mfma_f32_16x16x32_f16 v[198:201], v[10:13], v[206:209], v[198:201]
	v_mfma_f32_16x16x32_f16 v[202:205], v[14:17], v[206:209], v[202:205]
	s_waitcnt lgkmcnt(0)
	ds_read_b128 v[206:209], v242 offset:8832
	v_mfma_f32_16x16x32_f16 v[190:193], v[18:21], v[210:213], v[190:193]
	v_mfma_f32_16x16x32_f16 v[194:197], v[22:25], v[210:213], v[194:197]
	v_mfma_f32_16x16x32_f16 v[198:201], v[26:29], v[210:213], v[198:201]
	v_exp_f32_e32 v174, v174
	v_exp_f32_e32 v175, v175
	v_mfma_f32_16x16x32_f16 v[202:205], v[30:33], v[210:213], v[202:205]
	v_exp_f32_e32 v178, v178
	v_exp_f32_e32 v179, v179
	s_waitcnt lgkmcnt(0)
	ds_read_b128 v[210:213], v242 offset:8576
	v_mfma_f32_16x16x32_f16 v[190:193], v[214:217], v[206:209], v[190:193]
	ds_read_b128 v[214:217], v255 offset:4096
	v_exp_f32_e32 v182, v182
	v_exp_f32_e32 v183, v183
	v_mfma_f32_16x16x32_f16 v[194:197], v[218:221], v[206:209], v[194:197]
	ds_read_b128 v[218:221], v255 offset:5120
	v_exp_f32_e32 v186, v186
	v_exp_f32_e32 v187, v187
	v_add_f32_e32 v174, 1.0, v174
	v_mfma_f32_16x16x32_f16 v[198:201], v[222:225], v[206:209], v[198:201]
	ds_read_b128 v[222:225], v255 offset:6144
	v_add_f32_e32 v175, 1.0, v175
	v_add_f32_e32 v178, 1.0, v178
	v_mfma_f32_16x16x32_f16 v[202:205], v[226:229], v[206:209], v[202:205]
	ds_read_b128 v[226:229], v255 offset:7168
	v_add_f32_e32 v179, 1.0, v179
	v_add_f32_e32 v182, 1.0, v182
	s_waitcnt lgkmcnt(4)
	ds_read_b128 v[206:209], v242 offset:8640
	v_mfma_f32_16x16x32_f16 v[190:193], v[34:37], v[210:213], v[190:193]
	v_add_f32_e32 v183, 1.0, v183
	v_add_f32_e32 v186, 1.0, v186
	v_add_f32_e32 v187, 1.0, v187
	v_mfma_f32_16x16x32_f16 v[194:197], v[38:41], v[210:213], v[194:197]
	v_rcp_f32_e32 v174, v174
	v_rcp_f32_e32 v175, v175
	v_mfma_f32_16x16x32_f16 v[198:201], v[42:45], v[210:213], v[198:201]
	v_rcp_f32_e32 v178, v178
	v_rcp_f32_e32 v179, v179
	v_mfma_f32_16x16x32_f16 v[202:205], v[46:49], v[210:213], v[202:205]
	v_rcp_f32_e32 v182, v182
	v_rcp_f32_e32 v183, v183
	s_waitcnt lgkmcnt(0)
	ds_read_b128 v[210:213], v243 offset:4352
	v_mfma_f32_16x16x32_f16 v[190:193], v[50:53], v[206:209], v[190:193]
	v_rcp_f32_e32 v186, v186
	v_rcp_f32_e32 v187, v187
	v_fma_f32 v182, v182, s16, v252
	v_mfma_f32_16x16x32_f16 v[194:197], v[54:57], v[206:209], v[194:197]
	v_fma_f32 v183, v183, s16, v252
	v_mul_f32_e32 v174, v174, v182
	v_mfma_f32_16x16x32_f16 v[198:201], v[58:61], v[206:209], v[198:201]
	v_mul_f32_e32 v175, v175, v183
	v_fma_f32 v162, v178, v162, v174
	v_mfma_f32_16x16x32_f16 v[202:205], v[62:65], v[206:209], v[202:205]
	v_fma_f32 v163, v179, v163, v175
	v_exp_f32_e32 v178, v162
	v_exp_f32_e32 v179, v163
	s_waitcnt lgkmcnt(0)
	ds_read_b128 v[206:209], v243 offset:4416
	v_mfma_f32_16x16x32_f16 v[190:193], v[98:101], v[210:213], v[190:193]
	v_add_f32_e32 v178, 1.0, v178
	v_add_f32_e32 v179, 1.0, v179
	v_mfma_f32_16x16x32_f16 v[194:197], v[102:105], v[210:213], v[194:197]
	v_rcp_f32_e32 v178, v178
	v_rcp_f32_e32 v179, v179
	v_mfma_f32_16x16x32_f16 v[198:201], v[106:109], v[210:213], v[198:201]
	v_fma_f32 v178, v178, -2.0, 1.0
	v_fma_f32 v179, v179, -2.0, 1.0
	v_mfma_f32_16x16x32_f16 v[202:205], v[110:113], v[210:213], v[202:205]
	v_mul_f32_e32 v186, v186, v178
	v_mul_f32_e32 v187, v187, v179
	v_exp_f32_e32 v176, v176
	s_waitcnt lgkmcnt(0)
	ds_read_b128 v[210:213], v242 offset:8896
	v_mfma_f32_16x16x32_f16 v[190:193], v[114:117], v[206:209], v[190:193]
	v_exp_f32_e32 v177, v177
	v_exp_f32_e32 v180, v180
	v_mfma_f32_16x16x32_f16 v[194:197], v[118:121], v[206:209], v[194:197]
	v_exp_f32_e32 v181, v181
	v_exp_f32_e32 v184, v184
	v_mfma_f32_16x16x32_f16 v[198:201], v[122:125], v[206:209], v[198:201]
	v_exp_f32_e32 v185, v185
	v_exp_f32_e32 v188, v188
	v_exp_f32_e32 v189, v189
	v_mfma_f32_16x16x32_f16 v[202:205], v[126:129], v[206:209], v[202:205]
	v_add_f32_e32 v176, 1.0, v176
	v_add_f32_e32 v177, 1.0, v177
	s_waitcnt lgkmcnt(0)
	ds_read_b128 v[206:209], v242 offset:8704
	v_mfma_f32_16x16x32_f16 v[190:193], v[214:217], v[210:213], v[190:193]
	ds_read_b128 v[214:217], v255 offset:0
	v_add_f32_e32 v180, 1.0, v180
	v_add_f32_e32 v181, 1.0, v181
	v_mfma_f32_16x16x32_f16 v[194:197], v[218:221], v[210:213], v[194:197]
	ds_read_b128 v[218:221], v255 offset:1024
	v_add_f32_e32 v184, 1.0, v184
	v_add_f32_e32 v185, 1.0, v185
	v_mfma_f32_16x16x32_f16 v[198:201], v[222:225], v[210:213], v[198:201]
	ds_read_b128 v[222:225], v255 offset:2048
	v_add_f32_e32 v188, 1.0, v188
	v_add_f32_e32 v189, 1.0, v189
	v_rcp_f32_e32 v176, v176
	v_mfma_f32_16x16x32_f16 v[202:205], v[226:229], v[210:213], v[202:205]
	ds_read_b128 v[226:229], v255 offset:3072
	v_rcp_f32_e32 v177, v177
	v_rcp_f32_e32 v180, v180
	s_waitcnt lgkmcnt(4)
	ds_read_b128 v[210:213], v242 offset:8768
	v_mfma_f32_16x16x32_f16 v[190:193], v[66:69], v[206:209], v[190:193]
	v_rcp_f32_e32 v181, v181
	v_rcp_f32_e32 v184, v184
	v_mfma_f32_16x16x32_f16 v[194:197], v[70:73], v[206:209], v[194:197]
	v_rcp_f32_e32 v185, v185
	v_rcp_f32_e32 v188, v188
	v_rcp_f32_e32 v189, v189
	v_mfma_f32_16x16x32_f16 v[198:201], v[74:77], v[206:209], v[198:201]
	v_fma_f32 v184, v184, s16, v252
	v_fma_f32 v185, v185, s16, v252
	v_mfma_f32_16x16x32_f16 v[202:205], v[78:81], v[206:209], v[202:205]
	v_mul_f32_e32 v176, v176, v184
	v_mul_f32_e32 v177, v177, v185
	s_waitcnt lgkmcnt(0)
	ds_read_b128 v[206:209], v243 offset:4480
	v_mfma_f32_16x16x32_f16 v[190:193], v[82:85], v[210:213], v[190:193]
	v_fma_f32 v164, v180, v164, v176
	v_fma_f32 v165, v181, v165, v177
	v_mfma_f32_16x16x32_f16 v[194:197], v[86:89], v[210:213], v[194:197]
	v_exp_f32_e32 v180, v164
	v_exp_f32_e32 v181, v165
	v_add_f32_e32 v180, 1.0, v180
	v_mfma_f32_16x16x32_f16 v[198:201], v[90:93], v[210:213], v[198:201]
	v_add_f32_e32 v181, 1.0, v181
	v_rcp_f32_e32 v180, v180
	v_mfma_f32_16x16x32_f16 v[202:205], v[94:97], v[210:213], v[202:205]
	v_rcp_f32_e32 v181, v181
	v_fma_f32 v180, v180, -2.0, 1.0
	s_waitcnt lgkmcnt(0)
	ds_read_b128 v[210:213], v243 offset:4544
	v_mfma_f32_16x16x32_f16 v[190:193], v[130:133], v[206:209], v[190:193]
	v_fma_f32 v181, v181, -2.0, 1.0
	v_mul_f32_e32 v188, v188, v180
	v_mul_f32_e32 v189, v189, v181
	v_mfma_f32_16x16x32_f16 v[194:197], v[134:137], v[206:209], v[194:197]
	v_cvt_pk_f16_f32 v186, v186, v187
	v_cvt_pk_f16_f32 v187, v188, v189
	v_mfma_f32_16x16x32_f16 v[198:201], v[138:141], v[206:209], v[198:201]
	ds_write_b64 v244, v[186:187] offset:13056
	ds_read_b128 v[174:177], v245 offset:0
	v_mfma_f32_16x16x32_f16 v[202:205], v[142:145], v[206:209], v[202:205]
	ds_read_b128 v[178:181], v245 offset:512
	ds_read_b128 v[182:185], v245 offset:1024
	ds_read_b128 v[186:189], v245 offset:1536
	s_waitcnt lgkmcnt(5)
	ds_read_b128 v[206:209], v242 offset:16896
	v_mfma_f32_16x16x32_f16 v[190:193], v[146:149], v[210:213], v[190:193]
	v_mfma_f32_16x16x32_f16 v[194:197], v[150:153], v[210:213], v[194:197]
	v_mfma_f32_16x16x32_f16 v[198:201], v[154:157], v[210:213], v[198:201]
	v_mfma_f32_16x16x32_f16 v[202:205], v[158:161], v[210:213], v[202:205]
	s_waitcnt lgkmcnt(0)
	ds_read_b128 v[210:213], v242 offset:16960
	v_mfma_f32_16x16x32_f16 v[174:177], v[2:5], v[206:209], v[174:177]
	v_mfma_f32_16x16x32_f16 v[178:181], v[6:9], v[206:209], v[178:181]
	v_mfma_f32_16x16x32_f16 v[182:185], v[10:13], v[206:209], v[182:185]
	v_mfma_f32_16x16x32_f16 v[186:189], v[14:17], v[206:209], v[186:189]
	s_waitcnt lgkmcnt(0)
	ds_read_b128 v[206:209], v242 offset:17280
	v_mfma_f32_16x16x32_f16 v[174:177], v[18:21], v[210:213], v[174:177]
	v_mfma_f32_16x16x32_f16 v[178:181], v[22:25], v[210:213], v[178:181]
	v_mfma_f32_16x16x32_f16 v[182:185], v[26:29], v[210:213], v[182:185]
	s_waitcnt vmcnt(0)
	ds_write_b128 v249, v[230:233] offset:0
	ds_write_b128 v249, v[234:237] offset:33792
	ds_write_b128 v249, v[238:241] offset:42240
	v_exp_f32_e32 v190, v190
	v_mfma_f32_16x16x32_f16 v[186:189], v[30:33], v[210:213], v[186:189]
	v_exp_f32_e32 v191, v191
	v_exp_f32_e32 v194, v194
	s_waitcnt lgkmcnt(3)
	ds_read_b128 v[210:213], v242 offset:17024
	v_mfma_f32_16x16x32_f16 v[174:177], v[214:217], v[206:209], v[174:177]
	ds_read_b128 v[214:217], v255 offset:4096
	v_exp_f32_e32 v195, v195
	v_exp_f32_e32 v198, v198
	v_mfma_f32_16x16x32_f16 v[178:181], v[218:221], v[206:209], v[178:181]
	ds_read_b128 v[218:221], v255 offset:5120
	v_exp_f32_e32 v199, v199
	v_exp_f32_e32 v202, v202
	v_exp_f32_e32 v203, v203
	v_mfma_f32_16x16x32_f16 v[182:185], v[222:225], v[206:209], v[182:185]
	ds_read_b128 v[222:225], v255 offset:6144
	v_add_f32_e32 v190, 1.0, v190
	v_add_f32_e32 v191, 1.0, v191
	v_mfma_f32_16x16x32_f16 v[186:189], v[226:229], v[206:209], v[186:189]
	ds_read_b128 v[226:229], v255 offset:7168
	v_add_f32_e32 v194, 1.0, v194
	v_add_f32_e32 v195, 1.0, v195
	s_waitcnt lgkmcnt(4)
	ds_read_b128 v[206:209], v242 offset:17088
	v_mfma_f32_16x16x32_f16 v[174:177], v[34:37], v[210:213], v[174:177]
	v_add_f32_e32 v198, 1.0, v198
	v_add_f32_e32 v199, 1.0, v199
	v_add_f32_e32 v202, 1.0, v202
	v_mfma_f32_16x16x32_f16 v[178:181], v[38:41], v[210:213], v[178:181]
	v_add_f32_e32 v203, 1.0, v203
	v_rcp_f32_e32 v190, v190
	v_mfma_f32_16x16x32_f16 v[182:185], v[42:45], v[210:213], v[182:185]
	v_rcp_f32_e32 v191, v191
	v_rcp_f32_e32 v194, v194
	v_mfma_f32_16x16x32_f16 v[186:189], v[46:49], v[210:213], v[186:189]
	v_rcp_f32_e32 v195, v195
	v_rcp_f32_e32 v198, v198
	v_rcp_f32_e32 v199, v199
	s_waitcnt lgkmcnt(0)
	ds_read_b128 v[210:213], v243 offset:8704
	v_mfma_f32_16x16x32_f16 v[174:177], v[50:53], v[206:209], v[174:177]
	v_rcp_f32_e32 v202, v202
	v_rcp_f32_e32 v203, v203
	v_mfma_f32_16x16x32_f16 v[178:181], v[54:57], v[206:209], v[178:181]
	v_fma_f32 v198, v198, s16, v252
	v_fma_f32 v199, v199, s16, v252
	v_mfma_f32_16x16x32_f16 v[182:185], v[58:61], v[206:209], v[182:185]
	v_mul_f32_e32 v190, v190, v198
	v_mul_f32_e32 v191, v191, v199
	v_fma_f32 v166, v194, v166, v190
	v_mfma_f32_16x16x32_f16 v[186:189], v[62:65], v[206:209], v[186:189]
	v_fma_f32 v167, v195, v167, v191
	v_exp_f32_e32 v194, v166
	s_waitcnt lgkmcnt(0)
	ds_read_b128 v[206:209], v243 offset:8768
	v_mfma_f32_16x16x32_f16 v[174:177], v[98:101], v[210:213], v[174:177]
	v_exp_f32_e32 v195, v167
	v_add_f32_e32 v194, 1.0, v194
	v_mfma_f32_16x16x32_f16 v[178:181], v[102:105], v[210:213], v[178:181]
	v_add_f32_e32 v195, 1.0, v195
	v_rcp_f32_e32 v194, v194
	v_rcp_f32_e32 v195, v195
	v_mfma_f32_16x16x32_f16 v[182:185], v[106:109], v[210:213], v[182:185]
	v_fma_f32 v194, v194, -2.0, 1.0
	v_fma_f32 v195, v195, -2.0, 1.0
	v_mfma_f32_16x16x32_f16 v[186:189], v[110:113], v[210:213], v[186:189]
	v_mul_f32_e32 v202, v202, v194
	v_mul_f32_e32 v203, v203, v195
	s_waitcnt lgkmcnt(0)
	ds_read_b128 v[210:213], v242 offset:17344
	v_mfma_f32_16x16x32_f16 v[174:177], v[114:117], v[206:209], v[174:177]
	v_exp_f32_e32 v192, v192
	v_exp_f32_e32 v193, v193
	v_exp_f32_e32 v196, v196
	v_mfma_f32_16x16x32_f16 v[178:181], v[118:121], v[206:209], v[178:181]
	v_exp_f32_e32 v197, v197
	v_exp_f32_e32 v200, v200
	v_mfma_f32_16x16x32_f16 v[182:185], v[122:125], v[206:209], v[182:185]
	v_exp_f32_e32 v201, v201
	v_exp_f32_e32 v204, v204
	v_mfma_f32_16x16x32_f16 v[186:189], v[126:129], v[206:209], v[186:189]
	v_exp_f32_e32 v205, v205
	v_add_f32_e32 v192, 1.0, v192
	s_waitcnt lgkmcnt(0)
	ds_read_b128 v[206:209], v242 offset:17152
	v_mfma_f32_16x16x32_f16 v[174:177], v[214:217], v[210:213], v[174:177]
	ds_read_b128 v[214:217], v255 offset:0
	v_add_f32_e32 v193, 1.0, v193
	v_add_f32_e32 v196, 1.0, v196
	v_add_f32_e32 v197, 1.0, v197
	v_mfma_f32_16x16x32_f16 v[178:181], v[218:221], v[210:213], v[178:181]
	ds_read_b128 v[218:221], v255 offset:1024
	v_add_f32_e32 v200, 1.0, v200
	v_add_f32_e32 v201, 1.0, v201
	v_mfma_f32_16x16x32_f16 v[182:185], v[222:225], v[210:213], v[182:185]
	ds_read_b128 v[222:225], v255 offset:2048
	v_add_f32_e32 v204, 1.0, v204
	v_add_f32_e32 v205, 1.0, v205
	v_mfma_f32_16x16x32_f16 v[186:189], v[226:229], v[210:213], v[186:189]
	ds_read_b128 v[226:229], v255 offset:3072
	v_rcp_f32_e32 v192, v192
	v_rcp_f32_e32 v193, v193
	v_rcp_f32_e32 v196, v196
	s_waitcnt lgkmcnt(4)
	ds_read_b128 v[210:213], v242 offset:17216
	v_mfma_f32_16x16x32_f16 v[174:177], v[66:69], v[206:209], v[174:177]
	v_rcp_f32_e32 v197, v197
	v_rcp_f32_e32 v200, v200
	v_mfma_f32_16x16x32_f16 v[178:181], v[70:73], v[206:209], v[178:181]
	v_rcp_f32_e32 v201, v201
	v_rcp_f32_e32 v204, v204
	v_mfma_f32_16x16x32_f16 v[182:185], v[74:77], v[206:209], v[182:185]
	v_rcp_f32_e32 v205, v205
	v_fma_f32 v200, v200, s16, v252
	v_fma_f32 v201, v201, s16, v252
	v_mfma_f32_16x16x32_f16 v[186:189], v[78:81], v[206:209], v[186:189]
	v_mul_f32_e32 v192, v192, v200
	v_mul_f32_e32 v193, v193, v201
	s_waitcnt lgkmcnt(0)
	ds_read_b128 v[206:209], v243 offset:8832
	v_mfma_f32_16x16x32_f16 v[174:177], v[82:85], v[210:213], v[174:177]
	v_fma_f32 v168, v196, v168, v192
	v_fma_f32 v169, v197, v169, v193
	v_mfma_f32_16x16x32_f16 v[178:181], v[86:89], v[210:213], v[178:181]
	v_exp_f32_e32 v196, v168
	v_exp_f32_e32 v197, v169
	v_add_f32_e32 v196, 1.0, v196
	v_mfma_f32_16x16x32_f16 v[182:185], v[90:93], v[210:213], v[182:185]
	v_add_f32_e32 v197, 1.0, v197
	v_rcp_f32_e32 v196, v196
	v_mfma_f32_16x16x32_f16 v[186:189], v[94:97], v[210:213], v[186:189]
	v_rcp_f32_e32 v197, v197
	v_fma_f32 v196, v196, -2.0, 1.0
	s_waitcnt lgkmcnt(0)
	ds_read_b128 v[210:213], v243 offset:8896
	v_mfma_f32_16x16x32_f16 v[174:177], v[130:133], v[206:209], v[174:177]
	v_fma_f32 v197, v197, -2.0, 1.0
	v_mul_f32_e32 v204, v204, v196
	v_mul_f32_e32 v205, v205, v197
	v_mfma_f32_16x16x32_f16 v[178:181], v[134:137], v[206:209], v[178:181]
	v_cvt_pk_f16_f32 v202, v202, v203
	v_cvt_pk_f16_f32 v203, v204, v205
	v_mfma_f32_16x16x32_f16 v[182:185], v[138:141], v[206:209], v[182:185]
	ds_write_b64 v244, v[202:203] offset:17408
	ds_read_b128 v[190:193], v245 offset:0
	v_mfma_f32_16x16x32_f16 v[186:189], v[142:145], v[206:209], v[186:189]
	ds_read_b128 v[194:197], v245 offset:512
	ds_read_b128 v[198:201], v245 offset:1024
	ds_read_b128 v[202:205], v245 offset:1536
	s_waitcnt lgkmcnt(5)
	ds_read_b128 v[206:209], v242 offset:25344
	v_mfma_f32_16x16x32_f16 v[174:177], v[146:149], v[210:213], v[174:177]
	v_mfma_f32_16x16x32_f16 v[178:181], v[150:153], v[210:213], v[178:181]
	v_mfma_f32_16x16x32_f16 v[182:185], v[154:157], v[210:213], v[182:185]
	v_mfma_f32_16x16x32_f16 v[186:189], v[158:161], v[210:213], v[186:189]
	s_waitcnt lgkmcnt(0)
	ds_read_b128 v[210:213], v242 offset:25408
	v_mfma_f32_16x16x32_f16 v[190:193], v[2:5], v[206:209], v[190:193]
	v_mfma_f32_16x16x32_f16 v[194:197], v[6:9], v[206:209], v[194:197]
	v_mfma_f32_16x16x32_f16 v[198:201], v[10:13], v[206:209], v[198:201]
	v_mfma_f32_16x16x32_f16 v[202:205], v[14:17], v[206:209], v[202:205]
	s_waitcnt lgkmcnt(0)
	ds_read_b128 v[206:209], v242 offset:25728
	v_mfma_f32_16x16x32_f16 v[190:193], v[18:21], v[210:213], v[190:193]
	v_mfma_f32_16x16x32_f16 v[194:197], v[22:25], v[210:213], v[194:197]
	v_mfma_f32_16x16x32_f16 v[198:201], v[26:29], v[210:213], v[198:201]
	v_exp_f32_e32 v174, v174
	v_exp_f32_e32 v175, v175
	v_exp_f32_e32 v178, v178
	v_mfma_f32_16x16x32_f16 v[202:205], v[30:33], v[210:213], v[202:205]
	v_exp_f32_e32 v179, v179
	v_exp_f32_e32 v182, v182
	v_exp_f32_e32 v183, v183
	v_exp_f32_e32 v186, v186
	s_waitcnt lgkmcnt(0)
	ds_read_b128 v[210:213], v242 offset:25472
	v_mfma_f32_16x16x32_f16 v[190:193], v[214:217], v[206:209], v[190:193]
	ds_read_b128 v[214:217], v255 offset:4096
	v_exp_f32_e32 v187, v187
	v_add_f32_e32 v174, 1.0, v174
	v_add_f32_e32 v175, 1.0, v175
	v_add_f32_e32 v178, 1.0, v178
	v_mfma_f32_16x16x32_f16 v[194:197], v[218:221], v[206:209], v[194:197]
	ds_read_b128 v[218:221], v255 offset:5120
	v_add_f32_e32 v179, 1.0, v179
	v_add_f32_e32 v182, 1.0, v182
	v_add_f32_e32 v183, 1.0, v183
	v_add_f32_e32 v186, 1.0, v186
	v_mfma_f32_16x16x32_f16 v[198:201], v[222:225], v[206:209], v[198:201]
	ds_read_b128 v[222:225], v255 offset:6144
	v_add_f32_e32 v187, 1.0, v187
	v_rcp_f32_e32 v174, v174
	v_rcp_f32_e32 v175, v175
	v_rcp_f32_e32 v178, v178
	v_mfma_f32_16x16x32_f16 v[202:205], v[226:229], v[206:209], v[202:205]
	ds_read_b128 v[226:229], v255 offset:7168
	v_rcp_f32_e32 v179, v179
	v_rcp_f32_e32 v182, v182
	v_rcp_f32_e32 v183, v183
	v_rcp_f32_e32 v186, v186
	s_waitcnt lgkmcnt(4)
	ds_read_b128 v[206:209], v242 offset:25536
	v_mfma_f32_16x16x32_f16 v[190:193], v[34:37], v[210:213], v[190:193]
	v_rcp_f32_e32 v187, v187
	v_fma_f32 v182, v182, s16, v252
	v_fma_f32 v183, v183, s16, v252
	v_mul_f32_e32 v174, v174, v182
	v_mfma_f32_16x16x32_f16 v[194:197], v[38:41], v[210:213], v[194:197]
	v_mul_f32_e32 v175, v175, v183
	v_fma_f32 v170, v178, v170, v174
	v_fma_f32 v171, v179, v171, v175
	v_exp_f32_e32 v178, v170
	v_mfma_f32_16x16x32_f16 v[198:201], v[42:45], v[210:213], v[198:201]
	v_exp_f32_e32 v179, v171
	v_add_f32_e32 v178, 1.0, v178
	v_add_f32_e32 v179, 1.0, v179
	v_rcp_f32_e32 v178, v178
	v_mfma_f32_16x16x32_f16 v[202:205], v[46:49], v[210:213], v[202:205]
	v_rcp_f32_e32 v179, v179
	v_fma_f32 v178, v178, -2.0, 1.0
	v_fma_f32 v179, v179, -2.0, 1.0
	v_mul_f32_e32 v186, v186, v178
	s_waitcnt lgkmcnt(0)
	ds_read_b128 v[210:213], v242 offset:25600
	v_mfma_f32_16x16x32_f16 v[190:193], v[50:53], v[206:209], v[190:193]
	v_mul_f32_e32 v187, v187, v179
	v_exp_f32_e32 v176, v176
	v_exp_f32_e32 v177, v177
	v_exp_f32_e32 v180, v180
	v_mfma_f32_16x16x32_f16 v[194:197], v[54:57], v[206:209], v[194:197]
	v_exp_f32_e32 v181, v181
	v_exp_f32_e32 v184, v184
	v_exp_f32_e32 v185, v185
	v_exp_f32_e32 v188, v188
	v_mfma_f32_16x16x32_f16 v[198:201], v[58:61], v[206:209], v[198:201]
	v_exp_f32_e32 v189, v189
	v_add_f32_e32 v176, 1.0, v176
	v_add_f32_e32 v177, 1.0, v177
	v_add_f32_e32 v180, 1.0, v180
	v_mfma_f32_16x16x32_f16 v[202:205], v[62:65], v[206:209], v[202:205]
	v_add_f32_e32 v181, 1.0, v181
	v_add_f32_e32 v184, 1.0, v184
	v_add_f32_e32 v185, 1.0, v185
	v_add_f32_e32 v188, 1.0, v188
	s_waitcnt lgkmcnt(0)
	ds_read_b128 v[206:209], v242 offset:25792
	v_mfma_f32_16x16x32_f16 v[190:193], v[66:69], v[210:213], v[190:193]
	v_add_f32_e32 v189, 1.0, v189
	v_rcp_f32_e32 v176, v176
	v_rcp_f32_e32 v177, v177
	v_rcp_f32_e32 v180, v180
	v_mfma_f32_16x16x32_f16 v[194:197], v[70:73], v[210:213], v[194:197]
	v_rcp_f32_e32 v181, v181
	v_rcp_f32_e32 v184, v184
	v_rcp_f32_e32 v185, v185
	v_rcp_f32_e32 v188, v188
	v_mfma_f32_16x16x32_f16 v[198:201], v[74:77], v[210:213], v[198:201]
	v_rcp_f32_e32 v189, v189
	v_fma_f32 v184, v184, s16, v252
	v_fma_f32 v185, v185, s16, v252
	v_mul_f32_e32 v176, v176, v184
	v_mfma_f32_16x16x32_f16 v[202:205], v[78:81], v[210:213], v[202:205]
	v_mul_f32_e32 v177, v177, v185
	v_fma_f32 v172, v180, v172, v176
	v_fma_f32 v173, v181, v173, v177
	v_exp_f32_e32 v180, v172
	s_waitcnt lgkmcnt(0)
	ds_read_b128 v[210:213], v242 offset:25664
	v_mfma_f32_16x16x32_f16 v[190:193], v[214:217], v[206:209], v[190:193]
	ds_read_b128 v[214:217], v255 offset:0
	v_exp_f32_e32 v181, v173
	v_add_f32_e32 v180, 1.0, v180
	v_add_f32_e32 v181, 1.0, v181
	v_rcp_f32_e32 v180, v180
	v_mfma_f32_16x16x32_f16 v[194:197], v[218:221], v[206:209], v[194:197]
	ds_read_b128 v[218:221], v255 offset:1024
	v_rcp_f32_e32 v181, v181
	v_fma_f32 v180, v180, -2.0, 1.0
	v_fma_f32 v181, v181, -2.0, 1.0
	v_mul_f32_e32 v188, v188, v180
	v_mfma_f32_16x16x32_f16 v[198:201], v[222:225], v[206:209], v[198:201]
	ds_read_b128 v[222:225], v255 offset:2048
	v_mul_f32_e32 v189, v189, v181
	v_cvt_pk_f16_f32 v186, v186, v187
	v_cvt_pk_f16_f32 v187, v188, v189
	ds_write_b64 v244, v[186:187] offset:21760
	v_mfma_f32_16x16x32_f16 v[202:205], v[226:229], v[206:209], v[202:205]
	ds_read_b128 v[226:229], v255 offset:3072
	ds_read_b128 v[174:177], v245 offset:0
	ds_read_b128 v[178:181], v245 offset:512
	ds_read_b128 v[182:185], v245 offset:1024
	ds_read_b128 v[186:189], v245 offset:1536
	s_waitcnt lgkmcnt(9)
	v_mfma_f32_16x16x32_f16 v[190:193], v[82:85], v[210:213], v[190:193]
	v_mfma_f32_16x16x32_f16 v[194:197], v[86:89], v[210:213], v[194:197]
	v_mfma_f32_16x16x32_f16 v[198:201], v[90:93], v[210:213], v[198:201]
	v_mfma_f32_16x16x32_f16 v[202:205], v[94:97], v[210:213], v[202:205]
	s_waitcnt lgkmcnt(0)
	s_barrier
	ds_read_b128 v[206:209], v243 offset:13056
	ds_read_b128 v[230:233], v250 offset:13056
	s_mov_b64 exec, s[20:21]
	ds_read_b128 v[234:237], v250 offset:21760
	s_mov_b64 exec, -1
	s_waitcnt lgkmcnt(2)
	ds_read_b128 v[210:213], v243 offset:13120
	v_mfma_f32_16x16x32_f16 v[190:193], v[98:101], v[206:209], v[190:193]
	v_mfma_f32_16x16x32_f16 v[194:197], v[102:105], v[206:209], v[194:197]
	v_mfma_f32_16x16x32_f16 v[198:201], v[106:109], v[206:209], v[198:201]
	v_mfma_f32_16x16x32_f16 v[202:205], v[110:113], v[206:209], v[202:205]
	s_waitcnt lgkmcnt(1)
	s_mov_b64 exec, s[18:19]
	global_store_dwordx4 v251, v[230:233], s[10:11]
	s_mov_b64 exec, s[20:21]
	global_store_dwordx4 v251, v[234:237], s[14:15]
	s_mov_b64 exec, -1
	s_add_u32 s10, s10, 0x271000
	s_addc_u32 s11, s11, 0
	s_add_u32 s14, s14, 0x271000
	s_addc_u32 s15, s15, 0
	s_waitcnt lgkmcnt(0)
	ds_read_b128 v[206:209], v243 offset:13184
	v_mfma_f32_16x16x32_f16 v[190:193], v[114:117], v[210:213], v[190:193]
	v_mfma_f32_16x16x32_f16 v[194:197], v[118:121], v[210:213], v[194:197]
	global_load_dwordx4 v[230:233], v246, s[12:13]
	v_mfma_f32_16x16x32_f16 v[198:201], v[122:125], v[210:213], v[198:201]
	v_mfma_f32_16x16x32_f16 v[202:205], v[126:129], v[210:213], v[202:205]
	global_load_dwordx4 v[234:237], v247, s[8:9]
	s_waitcnt lgkmcnt(0)
	ds_read_b128 v[210:213], v243 offset:13248
	v_mfma_f32_16x16x32_f16 v[190:193], v[130:133], v[206:209], v[190:193]
	global_load_dwordx4 v[238:241], v248, s[8:9]
	v_mfma_f32_16x16x32_f16 v[194:197], v[134:137], v[206:209], v[194:197]
	v_mfma_f32_16x16x32_f16 v[198:201], v[138:141], v[206:209], v[198:201]
	s_add_u32 s8, s8, 0x271000
	v_mfma_f32_16x16x32_f16 v[202:205], v[142:145], v[206:209], v[202:205]
	s_waitcnt lgkmcnt(0)
	ds_read_b128 v[206:209], v242 offset:33792
	v_mfma_f32_16x16x32_f16 v[190:193], v[146:149], v[210:213], v[190:193]
	s_addc_u32 s9, s9, 0
	v_mfma_f32_16x16x32_f16 v[194:197], v[150:153], v[210:213], v[194:197]
	v_mfma_f32_16x16x32_f16 v[198:201], v[154:157], v[210:213], v[198:201]
	s_add_u32 s12, s12, 0x271000
	v_mfma_f32_16x16x32_f16 v[202:205], v[158:161], v[210:213], v[202:205]
	s_addc_u32 s13, s13, 0
	s_waitcnt lgkmcnt(0)
	ds_read_b128 v[210:213], v242 offset:33856
	v_mfma_f32_16x16x32_f16 v[174:177], v[2:5], v[206:209], v[174:177]
	v_mfma_f32_16x16x32_f16 v[178:181], v[6:9], v[206:209], v[178:181]
	v_mfma_f32_16x16x32_f16 v[182:185], v[10:13], v[206:209], v[182:185]
	v_mfma_f32_16x16x32_f16 v[186:189], v[14:17], v[206:209], v[186:189]
	s_waitcnt lgkmcnt(0)
	ds_read_b128 v[206:209], v242 offset:34176
	v_mfma_f32_16x16x32_f16 v[174:177], v[18:21], v[210:213], v[174:177]
	v_mfma_f32_16x16x32_f16 v[178:181], v[22:25], v[210:213], v[178:181]
	v_mfma_f32_16x16x32_f16 v[182:185], v[26:29], v[210:213], v[182:185]
	v_exp_f32_e32 v190, v190
	v_exp_f32_e32 v191, v191
	v_mfma_f32_16x16x32_f16 v[186:189], v[30:33], v[210:213], v[186:189]
	v_exp_f32_e32 v194, v194
	v_exp_f32_e32 v195, v195
	s_waitcnt lgkmcnt(0)
	ds_read_b128 v[210:213], v242 offset:33920
	v_mfma_f32_16x16x32_f16 v[174:177], v[214:217], v[206:209], v[174:177]
	ds_read_b128 v[214:217], v255 offset:4096
	v_exp_f32_e32 v198, v198
	v_exp_f32_e32 v199, v199
	v_mfma_f32_16x16x32_f16 v[178:181], v[218:221], v[206:209], v[178:181]
	ds_read_b128 v[218:221], v255 offset:5120
	v_exp_f32_e32 v202, v202
	v_exp_f32_e32 v203, v203
	v_add_f32_e32 v190, 1.0, v190
	v_mfma_f32_16x16x32_f16 v[182:185], v[222:225], v[206:209], v[182:185]
	ds_read_b128 v[222:225], v255 offset:6144
	v_add_f32_e32 v191, 1.0, v191
	v_add_f32_e32 v194, 1.0, v194
	v_mfma_f32_16x16x32_f16 v[186:189], v[226:229], v[206:209], v[186:189]
	ds_read_b128 v[226:229], v255 offset:7168
	v_add_f32_e32 v195, 1.0, v195
	v_add_f32_e32 v198, 1.0, v198
	s_waitcnt lgkmcnt(4)
	ds_read_b128 v[206:209], v242 offset:33984
	v_mfma_f32_16x16x32_f16 v[174:177], v[34:37], v[210:213], v[174:177]
	v_add_f32_e32 v199, 1.0, v199
	v_add_f32_e32 v202, 1.0, v202
	v_add_f32_e32 v203, 1.0, v203
	v_mfma_f32_16x16x32_f16 v[178:181], v[38:41], v[210:213], v[178:181]
	v_rcp_f32_e32 v190, v190
	v_rcp_f32_e32 v191, v191
	v_mfma_f32_16x16x32_f16 v[182:185], v[42:45], v[210:213], v[182:185]
	v_rcp_f32_e32 v194, v194
	v_rcp_f32_e32 v195, v195
	v_mfma_f32_16x16x32_f16 v[186:189], v[46:49], v[210:213], v[186:189]
	v_rcp_f32_e32 v198, v198
	v_rcp_f32_e32 v199, v199
	s_waitcnt lgkmcnt(0)
	ds_read_b128 v[210:213], v243 offset:17408
	v_mfma_f32_16x16x32_f16 v[174:177], v[50:53], v[206:209], v[174:177]
	v_rcp_f32_e32 v202, v202
	v_rcp_f32_e32 v203, v203
	v_fma_f32 v198, v198, s16, v252
	v_mfma_f32_16x16x32_f16 v[178:181], v[54:57], v[206:209], v[178:181]
	v_fma_f32 v199, v199, s16, v252
	v_mul_f32_e32 v190, v190, v198
	v_mfma_f32_16x16x32_f16 v[182:185], v[58:61], v[206:209], v[182:185]
	v_mul_f32_e32 v191, v191, v199
	v_fma_f32 v162, v194, v162, v190
	v_mfma_f32_16x16x32_f16 v[186:189], v[62:65], v[206:209], v[186:189]
	v_fma_f32 v163, v195, v163, v191
	v_exp_f32_e32 v194, v162
	v_exp_f32_e32 v195, v163
	s_waitcnt lgkmcnt(0)
	ds_read_b128 v[206:209], v243 offset:17472
	v_mfma_f32_16x16x32_f16 v[174:177], v[98:101], v[210:213], v[174:177]
	v_add_f32_e32 v194, 1.0, v194
	v_add_f32_e32 v195, 1.0, v195
	v_mfma_f32_16x16x32_f16 v[178:181], v[102:105], v[210:213], v[178:181]
	v_rcp_f32_e32 v194, v194
	v_rcp_f32_e32 v195, v195
	v_mfma_f32_16x16x32_f16 v[182:185], v[106:109], v[210:213], v[182:185]
	v_fma_f32 v194, v194, -2.0, 1.0
	v_fma_f32 v195, v195, -2.0, 1.0
	v_mfma_f32_16x16x32_f16 v[186:189], v[110:113], v[210:213], v[186:189]
	v_mul_f32_e32 v202, v202, v194
	v_mul_f32_e32 v203, v203, v195
	v_exp_f32_e32 v192, v192
	s_waitcnt lgkmcnt(0)
	ds_read_b128 v[210:213], v242 offset:34240
	v_mfma_f32_16x16x32_f16 v[174:177], v[114:117], v[206:209], v[174:177]
	v_exp_f32_e32 v193, v193
	v_exp_f32_e32 v196, v196
	v_mfma_f32_16x16x32_f16 v[178:181], v[118:121], v[206:209], v[178:181]
	v_exp_f32_e32 v197, v197
	v_exp_f32_e32 v200, v200
	v_mfma_f32_16x16x32_f16 v[182:185], v[122:125], v[206:209], v[182:185]
	v_exp_f32_e32 v201, v201
	v_exp_f32_e32 v204, v204
	v_exp_f32_e32 v205, v205
	v_mfma_f32_16x16x32_f16 v[186:189], v[126:129], v[206:209], v[186:189]
	v_add_f32_e32 v192, 1.0, v192
	v_add_f32_e32 v193, 1.0, v193
	s_waitcnt lgkmcnt(0)
	ds_read_b128 v[206:209], v242 offset:34048
	v_mfma_f32_16x16x32_f16 v[174:177], v[214:217], v[210:213], v[174:177]
	ds_read_b128 v[214:217], v255 offset:0
	v_add_f32_e32 v196, 1.0, v196
	v_add_f32_e32 v197, 1.0, v197
	v_mfma_f32_16x16x32_f16 v[178:181], v[218:221], v[210:213], v[178:181]
	ds_read_b128 v[218:221], v255 offset:1024
	v_add_f32_e32 v200, 1.0, v200
	v_add_f32_e32 v201, 1.0, v201
	v_mfma_f32_16x16x32_f16 v[182:185], v[222:225], v[210:213], v[182:185]
	ds_read_b128 v[222:225], v255 offset:2048
	v_add_f32_e32 v204, 1.0, v204
	v_add_f32_e32 v205, 1.0, v205
	v_rcp_f32_e32 v192, v192
	v_mfma_f32_16x16x32_f16 v[186:189], v[226:229], v[210:213], v[186:189]
	ds_read_b128 v[226:229], v255 offset:3072
	v_rcp_f32_e32 v193, v193
	v_rcp_f32_e32 v196, v196
	s_waitcnt lgkmcnt(4)
	ds_read_b128 v[210:213], v242 offset:34112
	v_mfma_f32_16x16x32_f16 v[174:177], v[66:69], v[206:209], v[174:177]
	v_rcp_f32_e32 v197, v197
	v_rcp_f32_e32 v200, v200
	v_mfma_f32_16x16x32_f16 v[178:181], v[70:73], v[206:209], v[178:181]
	v_rcp_f32_e32 v201, v201
	v_rcp_f32_e32 v204, v204
	v_rcp_f32_e32 v205, v205
	v_mfma_f32_16x16x32_f16 v[182:185], v[74:77], v[206:209], v[182:185]
	v_fma_f32 v200, v200, s16, v252
	v_fma_f32 v201, v201, s16, v252
	v_mfma_f32_16x16x32_f16 v[186:189], v[78:81], v[206:209], v[186:189]
	v_mul_f32_e32 v192, v192, v200
	v_mul_f32_e32 v193, v193, v201
	s_waitcnt lgkmcnt(0)
	ds_read_b128 v[206:209], v243 offset:17536
	v_mfma_f32_16x16x32_f16 v[174:177], v[82:85], v[210:213], v[174:177]
	v_fma_f32 v164, v196, v164, v192
	v_fma_f32 v165, v197, v165, v193
	v_mfma_f32_16x16x32_f16 v[178:181], v[86:89], v[210:213], v[178:181]
	v_exp_f32_e32 v196, v164
	v_exp_f32_e32 v197, v165
	v_add_f32_e32 v196, 1.0, v196
	v_mfma_f32_16x16x32_f16 v[182:185], v[90:93], v[210:213], v[182:185]
	v_add_f32_e32 v197, 1.0, v197
	v_rcp_f32_e32 v196, v196
	v_mfma_f32_16x16x32_f16 v[186:189], v[94:97], v[210:213], v[186:189]
	v_rcp_f32_e32 v197, v197
	v_fma_f32 v196, v196, -2.0, 1.0
	s_waitcnt lgkmcnt(0)
	ds_read_b128 v[210:213], v243 offset:17600
	v_mfma_f32_16x16x32_f16 v[174:177], v[130:133], v[206:209], v[174:177]
	v_fma_f32 v197, v197, -2.0, 1.0
	v_mul_f32_e32 v204, v204, v196
	v_mul_f32_e32 v205, v205, v197
	v_mfma_f32_16x16x32_f16 v[178:181], v[134:137], v[206:209], v[178:181]
	v_cvt_pk_f16_f32 v202, v202, v203
	v_cvt_pk_f16_f32 v203, v204, v205
	v_mfma_f32_16x16x32_f16 v[182:185], v[138:141], v[206:209], v[182:185]
	ds_write_b64 v244, v[202:203] offset:0
	ds_read_b128 v[190:193], v245 offset:0
	v_mfma_f32_16x16x32_f16 v[186:189], v[142:145], v[206:209], v[186:189]
	ds_read_b128 v[194:197], v245 offset:512
	ds_read_b128 v[198:201], v245 offset:1024
	ds_read_b128 v[202:205], v245 offset:1536
	s_waitcnt lgkmcnt(5)
	ds_read_b128 v[206:209], v242 offset:42240
	v_mfma_f32_16x16x32_f16 v[174:177], v[146:149], v[210:213], v[174:177]
	v_mfma_f32_16x16x32_f16 v[178:181], v[150:153], v[210:213], v[178:181]
	v_mfma_f32_16x16x32_f16 v[182:185], v[154:157], v[210:213], v[182:185]
	v_mfma_f32_16x16x32_f16 v[186:189], v[158:161], v[210:213], v[186:189]
	s_waitcnt lgkmcnt(0)
	ds_read_b128 v[210:213], v242 offset:42304
	v_mfma_f32_16x16x32_f16 v[190:193], v[2:5], v[206:209], v[190:193]
	v_mfma_f32_16x16x32_f16 v[194:197], v[6:9], v[206:209], v[194:197]
	v_mfma_f32_16x16x32_f16 v[198:201], v[10:13], v[206:209], v[198:201]
	v_mfma_f32_16x16x32_f16 v[202:205], v[14:17], v[206:209], v[202:205]
	s_waitcnt lgkmcnt(0)
	ds_read_b128 v[206:209], v242 offset:42624
	v_mfma_f32_16x16x32_f16 v[190:193], v[18:21], v[210:213], v[190:193]
	v_mfma_f32_16x16x32_f16 v[194:197], v[22:25], v[210:213], v[194:197]
	v_mfma_f32_16x16x32_f16 v[198:201], v[26:29], v[210:213], v[198:201]
	s_waitcnt vmcnt(0)
	ds_write_b128 v249, v[230:233] offset:25344
	ds_write_b128 v249, v[234:237] offset:8448
	ds_write_b128 v249, v[238:241] offset:16896
	v_exp_f32_e32 v174, v174
	v_mfma_f32_16x16x32_f16 v[202:205], v[30:33], v[210:213], v[202:205]
	v_exp_f32_e32 v175, v175
	v_exp_f32_e32 v178, v178
	s_waitcnt lgkmcnt(3)
	ds_read_b128 v[210:213], v242 offset:42368
	v_mfma_f32_16x16x32_f16 v[190:193], v[214:217], v[206:209], v[190:193]
	ds_read_b128 v[214:217], v255 offset:4096
	v_exp_f32_e32 v179, v179
	v_exp_f32_e32 v182, v182
	v_mfma_f32_16x16x32_f16 v[194:197], v[218:221], v[206:209], v[194:197]
	ds_read_b128 v[218:221], v255 offset:5120
	v_exp_f32_e32 v183, v183
	v_exp_f32_e32 v186, v186
	v_exp_f32_e32 v187, v187
	v_mfma_f32_16x16x32_f16 v[198:201], v[222:225], v[206:209], v[198:201]
	ds_read_b128 v[222:225], v255 offset:6144
	v_add_f32_e32 v174, 1.0, v174
	v_add_f32_e32 v175, 1.0, v175
	v_mfma_f32_16x16x32_f16 v[202:205], v[226:229], v[206:209], v[202:205]
	ds_read_b128 v[226:229], v255 offset:7168
	v_add_f32_e32 v178, 1.0, v178
	v_add_f32_e32 v179, 1.0, v179
	s_waitcnt lgkmcnt(4)
	ds_read_b128 v[206:209], v242 offset:42432
	v_mfma_f32_16x16x32_f16 v[190:193], v[34:37], v[210:213], v[190:193]
	v_add_f32_e32 v182, 1.0, v182
	v_add_f32_e32 v183, 1.0, v183
	v_add_f32_e32 v186, 1.0, v186
	v_mfma_f32_16x16x32_f16 v[194:197], v[38:41], v[210:213], v[194:197]
	v_add_f32_e32 v187, 1.0, v187
	v_rcp_f32_e32 v174, v174
	v_mfma_f32_16x16x32_f16 v[198:201], v[42:45], v[210:213], v[198:201]
	v_rcp_f32_e32 v175, v175
	v_rcp_f32_e32 v178, v178
	v_mfma_f32_16x16x32_f16 v[202:205], v[46:49], v[210:213], v[202:205]
	v_rcp_f32_e32 v179, v179
	v_rcp_f32_e32 v182, v182
	v_rcp_f32_e32 v183, v183
	s_waitcnt lgkmcnt(0)
	ds_read_b128 v[210:213], v243 offset:21760
	v_mfma_f32_16x16x32_f16 v[190:193], v[50:53], v[206:209], v[190:193]
	v_rcp_f32_e32 v186, v186
	v_rcp_f32_e32 v187, v187
	v_mfma_f32_16x16x32_f16 v[194:197], v[54:57], v[206:209], v[194:197]
	v_fma_f32 v182, v182, s16, v252
	v_fma_f32 v183, v183, s16, v252
	v_mfma_f32_16x16x32_f16 v[198:201], v[58:61], v[206:209], v[198:201]
	v_mul_f32_e32 v174, v174, v182
	v_mul_f32_e32 v175, v175, v183
	v_fma_f32 v166, v178, v166, v174
	v_mfma_f32_16x16x32_f16 v[202:205], v[62:65], v[206:209], v[202:205]
	v_fma_f32 v167, v179, v167, v175
	v_exp_f32_e32 v178, v166
	s_waitcnt lgkmcnt(0)
	ds_read_b128 v[206:209], v243 offset:21824
	v_mfma_f32_16x16x32_f16 v[190:193], v[98:101], v[210:213], v[190:193]
	v_exp_f32_e32 v179, v167
	v_add_f32_e32 v178, 1.0, v178
	v_mfma_f32_16x16x32_f16 v[194:197], v[102:105], v[210:213], v[194:197]
	v_add_f32_e32 v179, 1.0, v179
	v_rcp_f32_e32 v178, v178
	v_rcp_f32_e32 v179, v179
	v_mfma_f32_16x16x32_f16 v[198:201], v[106:109], v[210:213], v[198:201]
	v_fma_f32 v178, v178, -2.0, 1.0
	v_fma_f32 v179, v179, -2.0, 1.0
	v_mfma_f32_16x16x32_f16 v[202:205], v[110:113], v[210:213], v[202:205]
	v_mul_f32_e32 v186, v186, v178
	v_mul_f32_e32 v187, v187, v179
	s_waitcnt lgkmcnt(0)
	ds_read_b128 v[210:213], v242 offset:42688
	v_mfma_f32_16x16x32_f16 v[190:193], v[114:117], v[206:209], v[190:193]
	v_exp_f32_e32 v176, v176
	v_exp_f32_e32 v177, v177
	v_exp_f32_e32 v180, v180
	v_mfma_f32_16x16x32_f16 v[194:197], v[118:121], v[206:209], v[194:197]
	v_exp_f32_e32 v181, v181
	v_exp_f32_e32 v184, v184
	v_mfma_f32_16x16x32_f16 v[198:201], v[122:125], v[206:209], v[198:201]
	v_exp_f32_e32 v185, v185
	v_exp_f32_e32 v188, v188
	v_mfma_f32_16x16x32_f16 v[202:205], v[126:129], v[206:209], v[202:205]
	v_exp_f32_e32 v189, v189
	v_add_f32_e32 v176, 1.0, v176
	s_waitcnt lgkmcnt(0)
	ds_read_b128 v[206:209], v242 offset:42496
	v_mfma_f32_16x16x32_f16 v[190:193], v[214:217], v[210:213], v[190:193]
	ds_read_b128 v[214:217], v255 offset:0
	v_add_f32_e32 v177, 1.0, v177
	v_add_f32_e32 v180, 1.0, v180
	v_add_f32_e32 v181, 1.0, v181
	v_mfma_f32_16x16x32_f16 v[194:197], v[218:221], v[210:213], v[194:197]
	ds_read_b128 v[218:221], v255 offset:1024
	v_add_f32_e32 v184, 1.0, v184
	v_add_f32_e32 v185, 1.0, v185
	v_mfma_f32_16x16x32_f16 v[198:201], v[222:225], v[210:213], v[198:201]
	ds_read_b128 v[222:225], v255 offset:2048
	v_add_f32_e32 v188, 1.0, v188
	v_add_f32_e32 v189, 1.0, v189
	v_mfma_f32_16x16x32_f16 v[202:205], v[226:229], v[210:213], v[202:205]
	ds_read_b128 v[226:229], v255 offset:3072
	v_rcp_f32_e32 v176, v176
	v_rcp_f32_e32 v177, v177
	v_rcp_f32_e32 v180, v180
	s_waitcnt lgkmcnt(4)
	ds_read_b128 v[210:213], v242 offset:42560
	v_mfma_f32_16x16x32_f16 v[190:193], v[66:69], v[206:209], v[190:193]
	v_rcp_f32_e32 v181, v181
	v_rcp_f32_e32 v184, v184
	v_mfma_f32_16x16x32_f16 v[194:197], v[70:73], v[206:209], v[194:197]
	v_rcp_f32_e32 v185, v185
	v_rcp_f32_e32 v188, v188
	v_mfma_f32_16x16x32_f16 v[198:201], v[74:77], v[206:209], v[198:201]
	v_rcp_f32_e32 v189, v189
	v_fma_f32 v184, v184, s16, v252
	v_fma_f32 v185, v185, s16, v252
	v_mfma_f32_16x16x32_f16 v[202:205], v[78:81], v[206:209], v[202:205]
	v_mul_f32_e32 v176, v176, v184
	v_mul_f32_e32 v177, v177, v185
	s_waitcnt lgkmcnt(0)
	ds_read_b128 v[206:209], v243 offset:21888
	v_mfma_f32_16x16x32_f16 v[190:193], v[82:85], v[210:213], v[190:193]
	v_fma_f32 v168, v180, v168, v176
	v_fma_f32 v169, v181, v169, v177
	v_mfma_f32_16x16x32_f16 v[194:197], v[86:89], v[210:213], v[194:197]
	v_exp_f32_e32 v180, v168
	v_exp_f32_e32 v181, v169
	v_add_f32_e32 v180, 1.0, v180
	v_mfma_f32_16x16x32_f16 v[198:201], v[90:93], v[210:213], v[198:201]
	v_add_f32_e32 v181, 1.0, v181
	v_rcp_f32_e32 v180, v180
	v_mfma_f32_16x16x32_f16 v[202:205], v[94:97], v[210:213], v[202:205]
	v_rcp_f32_e32 v181, v181
	v_fma_f32 v180, v180, -2.0, 1.0
	s_waitcnt lgkmcnt(0)
	ds_read_b128 v[210:213], v243 offset:21952
	v_mfma_f32_16x16x32_f16 v[190:193], v[130:133], v[206:209], v[190:193]
	v_fma_f32 v181, v181, -2.0, 1.0
	v_mul_f32_e32 v188, v188, v180
	v_mul_f32_e32 v189, v189, v181
	v_mfma_f32_16x16x32_f16 v[194:197], v[134:137], v[206:209], v[194:197]
	v_cvt_pk_f16_f32 v186, v186, v187
	v_cvt_pk_f16_f32 v187, v188, v189
	v_mfma_f32_16x16x32_f16 v[198:201], v[138:141], v[206:209], v[198:201]
	ds_write_b64 v244, v[186:187] offset:4352
	ds_read_b128 v[174:177], v245 offset:0
	v_mfma_f32_16x16x32_f16 v[202:205], v[142:145], v[206:209], v[202:205]
	ds_read_b128 v[178:181], v245 offset:512
	ds_read_b128 v[182:185], v245 offset:1024
	ds_read_b128 v[186:189], v245 offset:1536
	s_waitcnt lgkmcnt(5)
	ds_read_b128 v[206:209], v242 offset:0
	v_mfma_f32_16x16x32_f16 v[190:193], v[146:149], v[210:213], v[190:193]
	v_mfma_f32_16x16x32_f16 v[194:197], v[150:153], v[210:213], v[194:197]
	v_mfma_f32_16x16x32_f16 v[198:201], v[154:157], v[210:213], v[198:201]
	v_mfma_f32_16x16x32_f16 v[202:205], v[158:161], v[210:213], v[202:205]
	s_waitcnt lgkmcnt(0)
	ds_read_b128 v[210:213], v242 offset:64
	v_mfma_f32_16x16x32_f16 v[174:177], v[2:5], v[206:209], v[174:177]
	v_mfma_f32_16x16x32_f16 v[178:181], v[6:9], v[206:209], v[178:181]
	v_mfma_f32_16x16x32_f16 v[182:185], v[10:13], v[206:209], v[182:185]
	v_mfma_f32_16x16x32_f16 v[186:189], v[14:17], v[206:209], v[186:189]
	s_waitcnt lgkmcnt(0)
	ds_read_b128 v[206:209], v242 offset:384
	v_mfma_f32_16x16x32_f16 v[174:177], v[18:21], v[210:213], v[174:177]
	v_mfma_f32_16x16x32_f16 v[178:181], v[22:25], v[210:213], v[178:181]
	v_mfma_f32_16x16x32_f16 v[182:185], v[26:29], v[210:213], v[182:185]
	v_exp_f32_e32 v190, v190
	v_exp_f32_e32 v191, v191
	v_exp_f32_e32 v194, v194
	v_mfma_f32_16x16x32_f16 v[186:189], v[30:33], v[210:213], v[186:189]
	v_exp_f32_e32 v195, v195
	v_exp_f32_e32 v198, v198
	v_exp_f32_e32 v199, v199
	v_exp_f32_e32 v202, v202
	s_waitcnt lgkmcnt(0)
	ds_read_b128 v[210:213], v242 offset:128
	v_mfma_f32_16x16x32_f16 v[174:177], v[214:217], v[206:209], v[174:177]
	ds_read_b128 v[214:217], v255 offset:4096
	v_exp_f32_e32 v203, v203
	v_add_f32_e32 v190, 1.0, v190
	v_add_f32_e32 v191, 1.0, v191
	v_add_f32_e32 v194, 1.0, v194
	v_mfma_f32_16x16x32_f16 v[178:181], v[218:221], v[206:209], v[178:181]
	ds_read_b128 v[218:221], v255 offset:5120
	v_add_f32_e32 v195, 1.0, v195
	v_add_f32_e32 v198, 1.0, v198
	v_add_f32_e32 v199, 1.0, v199
	v_add_f32_e32 v202, 1.0, v202
	v_mfma_f32_16x16x32_f16 v[182:185], v[222:225], v[206:209], v[182:185]
	ds_read_b128 v[222:225], v255 offset:6144
	v_add_f32_e32 v203, 1.0, v203
	v_rcp_f32_e32 v190, v190
	v_rcp_f32_e32 v191, v191
	v_rcp_f32_e32 v194, v194
	v_mfma_f32_16x16x32_f16 v[186:189], v[226:229], v[206:209], v[186:189]
	ds_read_b128 v[226:229], v255 offset:7168
	v_rcp_f32_e32 v195, v195
	v_rcp_f32_e32 v198, v198
	v_rcp_f32_e32 v199, v199
	v_rcp_f32_e32 v202, v202
	s_waitcnt lgkmcnt(4)
	ds_read_b128 v[206:209], v242 offset:192
	v_mfma_f32_16x16x32_f16 v[174:177], v[34:37], v[210:213], v[174:177]
	v_rcp_f32_e32 v203, v203
	v_fma_f32 v198, v198, s16, v252
	v_fma_f32 v199, v199, s16, v252
	v_mul_f32_e32 v190, v190, v198
	v_mfma_f32_16x16x32_f16 v[178:181], v[38:41], v[210:213], v[178:181]
	v_mul_f32_e32 v191, v191, v199
	v_fma_f32 v170, v194, v170, v190
	v_fma_f32 v171, v195, v171, v191
	v_exp_f32_e32 v194, v170
	v_mfma_f32_16x16x32_f16 v[182:185], v[42:45], v[210:213], v[182:185]
	v_exp_f32_e32 v195, v171
	v_add_f32_e32 v194, 1.0, v194
	v_add_f32_e32 v195, 1.0, v195
	v_rcp_f32_e32 v194, v194
	v_mfma_f32_16x16x32_f16 v[186:189], v[46:49], v[210:213], v[186:189]
	v_rcp_f32_e32 v195, v195
	v_fma_f32 v194, v194, -2.0, 1.0
	v_fma_f32 v195, v195, -2.0, 1.0
	v_mul_f32_e32 v202, v202, v194
	s_waitcnt lgkmcnt(0)
	ds_read_b128 v[210:213], v242 offset:256
	v_mfma_f32_16x16x32_f16 v[174:177], v[50:53], v[206:209], v[174:177]
	v_mul_f32_e32 v203, v203, v195
	v_exp_f32_e32 v192, v192
	v_exp_f32_e32 v193, v193
	v_exp_f32_e32 v196, v196
	v_mfma_f32_16x16x32_f16 v[178:181], v[54:57], v[206:209], v[178:181]
	v_exp_f32_e32 v197, v197
	v_exp_f32_e32 v200, v200
	v_exp_f32_e32 v201, v201
	v_exp_f32_e32 v204, v204
	v_mfma_f32_16x16x32_f16 v[182:185], v[58:61], v[206:209], v[182:185]
	v_exp_f32_e32 v205, v205
	v_add_f32_e32 v192, 1.0, v192
	v_add_f32_e32 v193, 1.0, v193
	v_add_f32_e32 v196, 1.0, v196
	v_mfma_f32_16x16x32_f16 v[186:189], v[62:65], v[206:209], v[186:189]
	v_add_f32_e32 v197, 1.0, v197
	v_add_f32_e32 v200, 1.0, v200
	v_add_f32_e32 v201, 1.0, v201
	v_add_f32_e32 v204, 1.0, v204
	s_waitcnt lgkmcnt(0)
	ds_read_b128 v[206:209], v242 offset:448
	v_mfma_f32_16x16x32_f16 v[174:177], v[66:69], v[210:213], v[174:177]
	v_add_f32_e32 v205, 1.0, v205
	v_rcp_f32_e32 v192, v192
	v_rcp_f32_e32 v193, v193
	v_rcp_f32_e32 v196, v196
	v_mfma_f32_16x16x32_f16 v[178:181], v[70:73], v[210:213], v[178:181]
	v_rcp_f32_e32 v197, v197
	v_rcp_f32_e32 v200, v200
	v_rcp_f32_e32 v201, v201
	v_rcp_f32_e32 v204, v204
	v_mfma_f32_16x16x32_f16 v[182:185], v[74:77], v[210:213], v[182:185]
	v_rcp_f32_e32 v205, v205
	v_fma_f32 v200, v200, s16, v252
	v_fma_f32 v201, v201, s16, v252
	v_mul_f32_e32 v192, v192, v200
	v_mfma_f32_16x16x32_f16 v[186:189], v[78:81], v[210:213], v[186:189]
	v_mul_f32_e32 v193, v193, v201
	v_fma_f32 v172, v196, v172, v192
	v_fma_f32 v173, v197, v173, v193
	v_exp_f32_e32 v196, v172
	s_waitcnt lgkmcnt(0)
	ds_read_b128 v[210:213], v242 offset:320
	v_mfma_f32_16x16x32_f16 v[174:177], v[214:217], v[206:209], v[174:177]
	ds_read_b128 v[214:217], v255 offset:0
	v_exp_f32_e32 v197, v173
	v_add_f32_e32 v196, 1.0, v196
	v_add_f32_e32 v197, 1.0, v197
	v_rcp_f32_e32 v196, v196
	v_mfma_f32_16x16x32_f16 v[178:181], v[218:221], v[206:209], v[178:181]
	ds_read_b128 v[218:221], v255 offset:1024
	v_rcp_f32_e32 v197, v197
	v_fma_f32 v196, v196, -2.0, 1.0
	v_fma_f32 v197, v197, -2.0, 1.0
	v_mul_f32_e32 v204, v204, v196
	v_mfma_f32_16x16x32_f16 v[182:185], v[222:225], v[206:209], v[182:185]
	ds_read_b128 v[222:225], v255 offset:2048
	v_mul_f32_e32 v205, v205, v197
	v_cvt_pk_f16_f32 v202, v202, v203
	v_cvt_pk_f16_f32 v203, v204, v205
	ds_write_b64 v244, v[202:203] offset:8704
	v_mfma_f32_16x16x32_f16 v[186:189], v[226:229], v[206:209], v[186:189]
	ds_read_b128 v[226:229], v255 offset:3072
	ds_read_b128 v[190:193], v245 offset:0
	ds_read_b128 v[194:197], v245 offset:512
	ds_read_b128 v[198:201], v245 offset:1024
	ds_read_b128 v[202:205], v245 offset:1536
	s_waitcnt lgkmcnt(9)
	v_mfma_f32_16x16x32_f16 v[174:177], v[82:85], v[210:213], v[174:177]
	v_mfma_f32_16x16x32_f16 v[178:181], v[86:89], v[210:213], v[178:181]
	v_mfma_f32_16x16x32_f16 v[182:185], v[90:93], v[210:213], v[182:185]
	v_mfma_f32_16x16x32_f16 v[186:189], v[94:97], v[210:213], v[186:189]
	s_waitcnt lgkmcnt(0)
	s_barrier
	s_add_u32 s17, s17, 2
	s_cmp_lt_u32 s17, 16
	s_cbranch_scc1 .Llstm1_loop
	ds_read_b128 v[230:233], v250
	s_mov_b64 exec, s[20:21]
	ds_read_b128 v[234:237], v250 offset:8704
	s_mov_b64 exec, -1
	s_waitcnt lgkmcnt(0)
	s_mov_b64 exec, s[18:19]
	global_store_dwordx4 v251, v[230:233], s[10:11]
	s_mov_b64 exec, s[20:21]
	global_store_dwordx4 v251, v[234:237], s[14:15]
	s_mov_b64 exec, -1
	s_branch .LBB6_39

	.section	.text._Z6k_lstmILi256ELi10ELb1ELb0EEvPKDF16_S1_S1_PKfPDF16_S1_S1_S1_S3_S3_S3_PfS5_,"axG",@progbits,_Z6k_lstmILi256ELi10ELb1ELb0EEvPKDF16_S1_S1_PKfPDF16_S1_S1_S1_S3_S3_S3_PfS5_,comdat
	.p2alignl 8, 3212836864

	.section	.text._Z6k_lstmILi128ELi8ELb0ELb1EEvPKDF16_S1_S1_PKfPDF16_S1_S1_S1_S3_S3_S3_PfS5_,"axG",@progbits,_Z6k_lstmILi128ELi8ELb0ELb1EEvPKDF16_S1_S1_PKfPDF16_S1_S1_S1_S3_S3_S3_PfS5_,comdat
	.p2alignl 8, 3212836864

	.text
	.p2alignl 8, 3212836864
	.fill 256, 4, 3212836864
